# grid barrier: last XCD leader releases all XGEN words directly (TOPGEN hop removed); non-leader inv back after poll
# baseline (speedup 1.0000x reference)
; __device__ __forceinline__ unsigned xb_ld(unsigned* p)              { return __hip_atomic_load(p, __ATOMIC_RELAXED, __HIP_MEMORY_SCOPE_AGENT); }
; __device__ __forceinline__ unsigned xb_add(unsigned* p, unsigned v) { return __hip_atomic_fetch_add(p, v, __ATOMIC_RELAXED, __HIP_MEMORY_SCOPE_AGENT); }
; #define XB_SPIN(cond, bar) do { unsigned _sp = 0; while (cond) { __builtin_amdgcn_s_sleep(1); \
;     if ((++_sp & 255u) == 0u) { if (xb_ld(&(bar)[XB_TMO])) break; if (_sp > XB_SPIN_CAP) { atomicAdd(&(bar)[XB_TMO], 1u); break; } } } } while (0)
; __device__ __forceinline__ void xcd_barrier(const XcdBarrier& b) {
;     ...
;         const unsigned old = xb_add(&bar[XB_XSUB(b.x)], 1u);
;         const unsigned gen = old / nloc;
;         if (old + 1u == (gen + 1u) * nloc) {
;             __builtin_amdgcn_fence(__ATOMIC_RELEASE, "agent");
;             asm volatile("s_waitcnt vmcnt(0)" ::: "memory");
;             const unsigned og = xb_add(&bar[XB_TOP], 1u);
;             const unsigned tg = og / nx;
;             if (og + 1u == (tg + 1u) * nx) xb_add(&bar[XB_TOPGEN], 1u);
;             else XB_SPIN(xb_ld(&bar[XB_TOPGEN]) == tg, bar);
;             __builtin_amdgcn_fence(__ATOMIC_ACQUIRE, "agent");
;             xb_add(&bar[XB_XGEN(b.x)], 1u);
;             asm volatile("s_waitcnt vmcnt(0)" ::: "memory");
;         } else {
;             XB_SPIN(xb_ld(&bar[XB_XGEN(b.x)]) == gen, bar);
.LBB0_671:
	s_or_b64 exec, exec, s[4:5]
	v_cvt_f32_u32_e32 v4, v2
	s_waitcnt vmcnt(0)
	v_readfirstlane_b32 s2, v3
	v_sub_u32_e32 v3, 0, v2
	v_rcp_iflag_f32_e32 v4, v4
	v_add_u32_e32 v5, s2, v1
	v_mul_f32_e32 v4, 0x4f7ffffe, v4
	v_cvt_u32_f32_e32 v4, v4
	v_mul_lo_u32 v1, v3, v4
	v_mul_hi_u32 v1, v4, v1
	v_add_u32_e32 v1, v4, v1
	v_mul_hi_u32 v1, v5, v1
	v_mul_lo_u32 v3, v1, v2
	v_sub_u32_e32 v3, v5, v3
	v_add_u32_e32 v4, 1, v1
	v_cmp_ge_u32_e32 vcc, v3, v2
	s_nop 1
	v_cndmask_b32_e32 v1, v1, v4, vcc
	v_sub_u32_e32 v4, v3, v2
	v_cndmask_b32_e32 v3, v3, v4, vcc
	v_add_u32_e32 v4, 1, v1
	v_cmp_ge_u32_e32 vcc, v3, v2
	v_add_u32_e32 v3, 1, v5
	s_nop 0
	v_cndmask_b32_e32 v1, v1, v4, vcc
	v_mul_lo_u32 v4, v2, v1
	v_add_u32_e32 v2, v4, v2
	v_cmp_ne_u32_e32 vcc, v3, v2
	s_and_saveexec_b64 s[2:3], vcc
	s_xor_b64 s[2:3], exec, s[2:3]
	s_cbranch_execz .LBB0_685
	s_add_i32 s44, s20, 0x900
	s_lshl_b64 s[4:5], s[44:45], 2
	s_add_u32 s6, s92, s4
	s_addc_u32 s7, s93, s5
	s_waitcnt lgkmcnt(0)
	global_load_dword v0, v65, s[6:7] sc1
	s_waitcnt vmcnt(0)
	v_cmp_eq_u32_e32 vcc, v0, v1
	s_and_saveexec_b64 s[4:5], vcc
	s_cbranch_execz .LBB0_684
	s_mov_b32 s18, 1
	s_mov_b64 s[8:9], 0
	s_branch .LBB0_675

; __device__ __forceinline__ unsigned xb_ld(unsigned* p)              { return __hip_atomic_load(p, __ATOMIC_RELAXED, __HIP_MEMORY_SCOPE_AGENT); }
; #define XB_SPIN(cond, bar) do { unsigned _sp = 0; while (cond) { __builtin_amdgcn_s_sleep(1); \
;     if ((++_sp & 255u) == 0u) { if (xb_ld(&(bar)[XB_TMO])) break; if (_sp > XB_SPIN_CAP) { atomicAdd(&(bar)[XB_TMO], 1u); break; } } } } while (0)
; __device__ __forceinline__ void xcd_barrier(const XcdBarrier& b) {
;     ...
;             XB_SPIN(xb_ld(&bar[XB_XGEN(b.x)]) == gen, bar);
;             __builtin_amdgcn_fence(__ATOMIC_ACQUIRE, "agent");
;             asm volatile("s_waitcnt vmcnt(0)" ::: "memory");
.LBB0_684:
	s_or_b64 exec, exec, s[4:5]
	s_waitcnt vmcnt(0)
	buffer_inv sc1
	s_waitcnt vmcnt(0)

; __device__ __forceinline__ unsigned xb_ld(unsigned* p)              { return __hip_atomic_load(p, __ATOMIC_RELAXED, __HIP_MEMORY_SCOPE_AGENT); }
; __device__ __forceinline__ unsigned xb_add(unsigned* p, unsigned v) { return __hip_atomic_fetch_add(p, v, __ATOMIC_RELAXED, __HIP_MEMORY_SCOPE_AGENT); }
; #define XB_SPIN(cond, bar) do { unsigned _sp = 0; while (cond) { __builtin_amdgcn_s_sleep(1); \
;     if ((++_sp & 255u) == 0u) { if (xb_ld(&(bar)[XB_TMO])) break; if (_sp > XB_SPIN_CAP) { atomicAdd(&(bar)[XB_TMO], 1u); break; } } } } while (0)
; __device__ __forceinline__ void xcd_barrier(const XcdBarrier& b) {
;     ...
;             __builtin_amdgcn_fence(__ATOMIC_RELEASE, "agent");
;             asm volatile("s_waitcnt vmcnt(0)" ::: "memory");
;             const unsigned og = xb_add(&bar[XB_TOP], 1u);
;             const unsigned tg = og / nx;
;             if (og + 1u == (tg + 1u) * nx) xb_add(&bar[XB_TOPGEN], 1u);
;             else XB_SPIN(xb_ld(&bar[XB_TOPGEN]) == tg, bar);
;             __builtin_amdgcn_fence(__ATOMIC_ACQUIRE, "agent");
;             xb_add(&bar[XB_XGEN(b.x)], 1u);
;             asm volatile("s_waitcnt vmcnt(0)" ::: "memory");
.LBB0_688:
	s_or_b64 exec, exec, s[4:5]
	s_waitcnt vmcnt(0)
	v_readfirstlane_b32 s2, v2
	v_cvt_f32_u32_e32 v2, v0
	v_sub_u32_e32 v3, 0, v0
	v_add_u32_e32 v1, s2, v1
	s_add_u32 s2, s92, 0x3500
	v_rcp_iflag_f32_e32 v2, v2
	s_addc_u32 s3, s93, 0
	s_mov_b64 s[6:7], -1
	v_mul_f32_e32 v2, 0x4f7ffffe, v2
	v_cvt_u32_f32_e32 v2, v2
	v_mul_lo_u32 v3, v3, v2
	v_mul_hi_u32 v3, v2, v3
	v_add_u32_e32 v2, v2, v3
	v_mul_hi_u32 v2, v1, v2
	v_mul_lo_u32 v3, v2, v0
	v_sub_u32_e32 v3, v1, v3
	v_cmp_ge_u32_e32 vcc, v3, v0
	v_add_u32_e32 v4, 1, v2
	v_add_u32_e32 v1, 1, v1
	v_cndmask_b32_e32 v2, v2, v4, vcc
	v_sub_u32_e32 v4, v3, v0
	v_cndmask_b32_e32 v3, v3, v4, vcc
	v_cmp_ge_u32_e32 vcc, v3, v0
	v_add_u32_e32 v3, 1, v2
	s_nop 0
	v_cndmask_b32_e32 v2, v2, v3, vcc
	v_mul_lo_u32 v3, v0, v2
	v_add_u32_e32 v0, v3, v0
	v_cmp_ne_u32_e32 vcc, v1, v0
	v_mov_b64_e32 v[0:1], s[2:3]
	s_cbranch_vccnz .Lxrel_skip_0
	v_mov_b32_e32 v3, 1
	v_mov_b32_e32 v4, 0x2400
	global_atomic_add v4, v3, s[92:93]
	global_atomic_add v4, v3, s[92:93] offset:256
	global_atomic_add v4, v3, s[92:93] offset:512
	global_atomic_add v4, v3, s[92:93] offset:768
	global_atomic_add v4, v3, s[92:93] offset:1024
	global_atomic_add v4, v3, s[92:93] offset:1280
	global_atomic_add v4, v3, s[92:93] offset:1536
	global_atomic_add v4, v3, s[92:93] offset:1792
	global_atomic_add v4, v3, s[92:93] offset:2048
	global_atomic_add v4, v3, s[92:93] offset:2304
	global_atomic_add v4, v3, s[92:93] offset:2560
	global_atomic_add v4, v3, s[92:93] offset:2816
	global_atomic_add v4, v3, s[92:93] offset:3072
	global_atomic_add v4, v3, s[92:93] offset:3328
	global_atomic_add v4, v3, s[92:93] offset:3584
	global_atomic_add v4, v3, s[92:93] offset:3840
.Lxrel_skip_0:
	s_and_saveexec_b64 s[4:5], vcc
	s_cbranch_execz .LBB0_700
	s_add_i32 s44, s20, 0x900
	s_lshl_b64 s[2:3], s[44:45], 2
	s_add_u32 s2, s92, s2
	s_addc_u32 s3, s93, s3
	global_load_dword v0, v65, s[2:3] sc1
	s_mov_b64 s[10:11], 0
	s_waitcnt vmcnt(0)
	v_cmp_eq_u32_e32 vcc, v0, v2
	s_and_saveexec_b64 s[8:9], vcc
	s_cbranch_execz .LBB0_699
	s_add_u32 s6, s92, 0x200
	s_addc_u32 s7, s93, 0
	s_mov_b32 s21, 1
	s_branch .LBB0_692

; __device__ __forceinline__ unsigned xb_ld(unsigned* p)              { return __hip_atomic_load(p, __ATOMIC_RELAXED, __HIP_MEMORY_SCOPE_AGENT); }
; __device__ __forceinline__ unsigned xb_add(unsigned* p, unsigned v) { return __hip_atomic_fetch_add(p, v, __ATOMIC_RELAXED, __HIP_MEMORY_SCOPE_AGENT); }
; #define XB_SPIN(cond, bar) do { unsigned _sp = 0; while (cond) { __builtin_amdgcn_s_sleep(1); \
;     if ((++_sp & 255u) == 0u) { if (xb_ld(&(bar)[XB_TMO])) break; if (_sp > XB_SPIN_CAP) { atomicAdd(&(bar)[XB_TMO], 1u); break; } } } } while (0)
; __device__ __forceinline__ void xcd_barrier(const XcdBarrier& b) {
;     ...
;             else XB_SPIN(xb_ld(&bar[XB_TOPGEN]) == tg, bar);
;             __builtin_amdgcn_fence(__ATOMIC_ACQUIRE, "agent");
;             xb_add(&bar[XB_XGEN(b.x)], 1u);
;             asm volatile("s_waitcnt vmcnt(0)" ::: "memory");
.LBB0_702:
	s_or_b64 exec, exec, s[2:3]
	s_mov_b64 s[2:3], exec
	v_mbcnt_lo_u32_b32 v0, s2, 0
	v_mbcnt_hi_u32_b32 v0, s3, v0
	v_cmp_eq_u32_e32 vcc, 0, v0
	s_waitcnt vmcnt(0)
	buffer_inv sc1
	s_and_saveexec_b64 s[4:5], vcc
	s_cbranch_execz .LBB0_704
	s_add_i32 s44, s20, 0x900
	s_lshl_b64 s[6:7], s[44:45], 2
	s_add_u32 s6, s92, s6
	s_addc_u32 s7, s93, s7
	s_bcnt1_i32_b64 s2, s[2:3]
	v_mov_b32_e32 v0, s2
.LBB0_704:
	s_or_b64 exec, exec, s[4:5]
	s_waitcnt vmcnt(0)

; __device__ __forceinline__ unsigned xb_ld(unsigned* p)              { return __hip_atomic_load(p, __ATOMIC_RELAXED, __HIP_MEMORY_SCOPE_AGENT); }
; __device__ __forceinline__ unsigned xb_add(unsigned* p, unsigned v) { return __hip_atomic_fetch_add(p, v, __ATOMIC_RELAXED, __HIP_MEMORY_SCOPE_AGENT); }
; #define XB_SPIN(cond, bar) do { unsigned _sp = 0; while (cond) { __builtin_amdgcn_s_sleep(1); \
;     if ((++_sp & 255u) == 0u) { if (xb_ld(&(bar)[XB_TMO])) break; if (_sp > XB_SPIN_CAP) { atomicAdd(&(bar)[XB_TMO], 1u); break; } } } } while (0)
; __device__ __forceinline__ void xcd_barrier(const XcdBarrier& b) {
;     ...
;         const unsigned old = xb_add(&bar[XB_XSUB(b.x)], 1u);
;         const unsigned gen = old / nloc;
;         if (old + 1u == (gen + 1u) * nloc) {
;             __builtin_amdgcn_fence(__ATOMIC_RELEASE, "agent");
;             asm volatile("s_waitcnt vmcnt(0)" ::: "memory");
;             const unsigned og = xb_add(&bar[XB_TOP], 1u);
;             const unsigned tg = og / nx;
;             if (og + 1u == (tg + 1u) * nx) xb_add(&bar[XB_TOPGEN], 1u);
;             else XB_SPIN(xb_ld(&bar[XB_TOPGEN]) == tg, bar);
;             __builtin_amdgcn_fence(__ATOMIC_ACQUIRE, "agent");
;             xb_add(&bar[XB_XGEN(b.x)], 1u);
;             asm volatile("s_waitcnt vmcnt(0)" ::: "memory");
;         } else {
;             XB_SPIN(xb_ld(&bar[XB_XGEN(b.x)]) == gen, bar);
.LBB0_743:
	s_or_b64 exec, exec, s[6:7]
	v_cvt_f32_u32_e32 v4, v2
	s_waitcnt vmcnt(0)
	v_readfirstlane_b32 s4, v3
	v_sub_u32_e32 v3, 0, v2
	v_rcp_iflag_f32_e32 v4, v4
	v_add_u32_e32 v5, s4, v1
	v_mul_f32_e32 v4, 0x4f7ffffe, v4
	v_cvt_u32_f32_e32 v4, v4
	v_mul_lo_u32 v1, v3, v4
	v_mul_hi_u32 v1, v4, v1
	v_add_u32_e32 v1, v4, v1
	v_mul_hi_u32 v1, v5, v1
	v_mul_lo_u32 v3, v1, v2
	v_sub_u32_e32 v3, v5, v3
	v_add_u32_e32 v4, 1, v1
	v_cmp_ge_u32_e32 vcc, v3, v2
	s_nop 1
	v_cndmask_b32_e32 v1, v1, v4, vcc
	v_sub_u32_e32 v4, v3, v2
	v_cndmask_b32_e32 v3, v3, v4, vcc
	v_add_u32_e32 v4, 1, v1
	v_cmp_ge_u32_e32 vcc, v3, v2
	v_add_u32_e32 v3, 1, v5
	s_nop 0
	v_cndmask_b32_e32 v1, v1, v4, vcc
	v_mul_lo_u32 v4, v2, v1
	v_add_u32_e32 v2, v4, v2
	v_cmp_ne_u32_e32 vcc, v3, v2
	s_and_saveexec_b64 s[4:5], vcc
	s_xor_b64 s[4:5], exec, s[4:5]
	s_cbranch_execz .LBB0_757
	s_add_i32 s44, s23, 0x900
	s_lshl_b64 s[6:7], s[44:45], 2
	s_add_u32 s8, s92, s6
	s_addc_u32 s9, s93, s7
	s_waitcnt lgkmcnt(0)
	global_load_dword v0, v65, s[8:9] sc1
	s_waitcnt vmcnt(0)
	v_cmp_eq_u32_e32 vcc, v0, v1
	s_and_saveexec_b64 s[6:7], vcc
	s_cbranch_execz .LBB0_756
	s_mov_b32 s20, 1
	s_mov_b64 s[10:11], 0
	s_branch .LBB0_747

; __device__ __forceinline__ unsigned xb_ld(unsigned* p)              { return __hip_atomic_load(p, __ATOMIC_RELAXED, __HIP_MEMORY_SCOPE_AGENT); }
; #define XB_SPIN(cond, bar) do { unsigned _sp = 0; while (cond) { __builtin_amdgcn_s_sleep(1); \
;     if ((++_sp & 255u) == 0u) { if (xb_ld(&(bar)[XB_TMO])) break; if (_sp > XB_SPIN_CAP) { atomicAdd(&(bar)[XB_TMO], 1u); break; } } } } while (0)
; __device__ __forceinline__ void xcd_barrier(const XcdBarrier& b) {
;     ...
;             XB_SPIN(xb_ld(&bar[XB_XGEN(b.x)]) == gen, bar);
;             __builtin_amdgcn_fence(__ATOMIC_ACQUIRE, "agent");
;             asm volatile("s_waitcnt vmcnt(0)" ::: "memory");
.LBB0_756:
	s_or_b64 exec, exec, s[6:7]
	s_waitcnt vmcnt(0)
	buffer_inv sc1
	s_waitcnt vmcnt(0)

; __device__ __forceinline__ unsigned xb_ld(unsigned* p)              { return __hip_atomic_load(p, __ATOMIC_RELAXED, __HIP_MEMORY_SCOPE_AGENT); }
; __device__ __forceinline__ unsigned xb_add(unsigned* p, unsigned v) { return __hip_atomic_fetch_add(p, v, __ATOMIC_RELAXED, __HIP_MEMORY_SCOPE_AGENT); }
; #define XB_SPIN(cond, bar) do { unsigned _sp = 0; while (cond) { __builtin_amdgcn_s_sleep(1); \
;     if ((++_sp & 255u) == 0u) { if (xb_ld(&(bar)[XB_TMO])) break; if (_sp > XB_SPIN_CAP) { atomicAdd(&(bar)[XB_TMO], 1u); break; } } } } while (0)
; __device__ __forceinline__ void xcd_barrier(const XcdBarrier& b) {
;     ...
;             __builtin_amdgcn_fence(__ATOMIC_RELEASE, "agent");
;             asm volatile("s_waitcnt vmcnt(0)" ::: "memory");
;             const unsigned og = xb_add(&bar[XB_TOP], 1u);
;             const unsigned tg = og / nx;
;             if (og + 1u == (tg + 1u) * nx) xb_add(&bar[XB_TOPGEN], 1u);
;             else XB_SPIN(xb_ld(&bar[XB_TOPGEN]) == tg, bar);
;             __builtin_amdgcn_fence(__ATOMIC_ACQUIRE, "agent");
;             xb_add(&bar[XB_XGEN(b.x)], 1u);
;             asm volatile("s_waitcnt vmcnt(0)" ::: "memory");
.LBB0_760:
	s_or_b64 exec, exec, s[6:7]
	s_waitcnt vmcnt(0)
	v_readfirstlane_b32 s4, v2
	v_cvt_f32_u32_e32 v2, v0
	v_sub_u32_e32 v3, 0, v0
	v_add_u32_e32 v1, s4, v1
	s_add_u32 s4, s92, 0x3500
	v_rcp_iflag_f32_e32 v2, v2
	s_addc_u32 s5, s93, 0
	s_mov_b64 s[8:9], -1
	v_mul_f32_e32 v2, 0x4f7ffffe, v2
	v_cvt_u32_f32_e32 v2, v2
	v_mul_lo_u32 v3, v3, v2
	v_mul_hi_u32 v3, v2, v3
	v_add_u32_e32 v2, v2, v3
	v_mul_hi_u32 v2, v1, v2
	v_mul_lo_u32 v3, v2, v0
	v_sub_u32_e32 v3, v1, v3
	v_cmp_ge_u32_e32 vcc, v3, v0
	v_add_u32_e32 v4, 1, v2
	v_add_u32_e32 v1, 1, v1
	v_cndmask_b32_e32 v2, v2, v4, vcc
	v_sub_u32_e32 v4, v3, v0
	v_cndmask_b32_e32 v3, v3, v4, vcc
	v_cmp_ge_u32_e32 vcc, v3, v0
	v_add_u32_e32 v3, 1, v2
	s_nop 0
	v_cndmask_b32_e32 v2, v2, v3, vcc
	v_mul_lo_u32 v3, v0, v2
	v_add_u32_e32 v0, v3, v0
	v_cmp_ne_u32_e32 vcc, v1, v0
	v_mov_b64_e32 v[0:1], s[4:5]
	s_cbranch_vccnz .Lxrel_skip_1
	v_mov_b32_e32 v3, 1
	v_mov_b32_e32 v4, 0x2400
	global_atomic_add v4, v3, s[92:93]
	global_atomic_add v4, v3, s[92:93] offset:256
	global_atomic_add v4, v3, s[92:93] offset:512
	global_atomic_add v4, v3, s[92:93] offset:768
	global_atomic_add v4, v3, s[92:93] offset:1024
	global_atomic_add v4, v3, s[92:93] offset:1280
	global_atomic_add v4, v3, s[92:93] offset:1536
	global_atomic_add v4, v3, s[92:93] offset:1792
	global_atomic_add v4, v3, s[92:93] offset:2048
	global_atomic_add v4, v3, s[92:93] offset:2304
	global_atomic_add v4, v3, s[92:93] offset:2560
	global_atomic_add v4, v3, s[92:93] offset:2816
	global_atomic_add v4, v3, s[92:93] offset:3072
	global_atomic_add v4, v3, s[92:93] offset:3328
	global_atomic_add v4, v3, s[92:93] offset:3584
	global_atomic_add v4, v3, s[92:93] offset:3840
.Lxrel_skip_1:
	s_and_saveexec_b64 s[6:7], vcc
	s_cbranch_execz .LBB0_772
	s_add_i32 s44, s23, 0x900
	s_lshl_b64 s[4:5], s[44:45], 2
	s_add_u32 s4, s92, s4
	s_addc_u32 s5, s93, s5
	global_load_dword v0, v65, s[4:5] sc1
	s_mov_b64 s[12:13], 0
	s_waitcnt vmcnt(0)
	v_cmp_eq_u32_e32 vcc, v0, v2
	s_and_saveexec_b64 s[10:11], vcc
	s_cbranch_execz .LBB0_771
	s_add_u32 s8, s92, 0x200
	s_addc_u32 s9, s93, 0
	s_mov_b32 s24, 1
	s_branch .LBB0_764

; __device__ __forceinline__ unsigned xb_ld(unsigned* p)              { return __hip_atomic_load(p, __ATOMIC_RELAXED, __HIP_MEMORY_SCOPE_AGENT); }
; __device__ __forceinline__ unsigned xb_add(unsigned* p, unsigned v) { return __hip_atomic_fetch_add(p, v, __ATOMIC_RELAXED, __HIP_MEMORY_SCOPE_AGENT); }
; #define XB_SPIN(cond, bar) do { unsigned _sp = 0; while (cond) { __builtin_amdgcn_s_sleep(1); \
;     if ((++_sp & 255u) == 0u) { if (xb_ld(&(bar)[XB_TMO])) break; if (_sp > XB_SPIN_CAP) { atomicAdd(&(bar)[XB_TMO], 1u); break; } } } } while (0)
; __device__ __forceinline__ void xcd_barrier(const XcdBarrier& b) {
;     ...
;             else XB_SPIN(xb_ld(&bar[XB_TOPGEN]) == tg, bar);
;             __builtin_amdgcn_fence(__ATOMIC_ACQUIRE, "agent");
;             xb_add(&bar[XB_XGEN(b.x)], 1u);
;             asm volatile("s_waitcnt vmcnt(0)" ::: "memory");
.LBB0_774:
	s_or_b64 exec, exec, s[4:5]
	s_mov_b64 s[4:5], exec
	v_mbcnt_lo_u32_b32 v0, s4, 0
	v_mbcnt_hi_u32_b32 v0, s5, v0
	v_cmp_eq_u32_e32 vcc, 0, v0
	s_waitcnt vmcnt(0)
	buffer_inv sc1
	s_and_saveexec_b64 s[6:7], vcc
	s_cbranch_execz .LBB0_776
	s_add_i32 s44, s23, 0x900
	s_lshl_b64 s[8:9], s[44:45], 2
	s_add_u32 s8, s92, s8
	s_addc_u32 s9, s93, s9
	s_bcnt1_i32_b64 s4, s[4:5]
	v_mov_b32_e32 v0, s4
.LBB0_776:
	s_or_b64 exec, exec, s[6:7]
	s_waitcnt vmcnt(0)

; __device__ __forceinline__ unsigned xb_ld(unsigned* p)              { return __hip_atomic_load(p, __ATOMIC_RELAXED, __HIP_MEMORY_SCOPE_AGENT); }
; __device__ __forceinline__ unsigned xb_add(unsigned* p, unsigned v) { return __hip_atomic_fetch_add(p, v, __ATOMIC_RELAXED, __HIP_MEMORY_SCOPE_AGENT); }
; #define XB_SPIN(cond, bar) do { unsigned _sp = 0; while (cond) { __builtin_amdgcn_s_sleep(1); \
;     if ((++_sp & 255u) == 0u) { if (xb_ld(&(bar)[XB_TMO])) break; if (_sp > XB_SPIN_CAP) { atomicAdd(&(bar)[XB_TMO], 1u); break; } } } } while (0)
; __device__ __forceinline__ void xcd_barrier(const XcdBarrier& b) {
;     ...
;             else XB_SPIN(xb_ld(&bar[XB_TOPGEN]) == tg, bar);
;             __builtin_amdgcn_fence(__ATOMIC_ACQUIRE, "agent");
;             xb_add(&bar[XB_XGEN(b.x)], 1u);
;             asm volatile("s_waitcnt vmcnt(0)" ::: "memory");
.LBB0_1219:
	s_or_b64 exec, exec, s[2:3]
	s_mov_b64 s[2:3], exec
	v_mbcnt_lo_u32_b32 v0, s2, 0
	v_mbcnt_hi_u32_b32 v0, s3, v0
	v_cmp_eq_u32_e32 vcc, 0, v0
	s_waitcnt vmcnt(0)
	buffer_inv sc1
	s_and_saveexec_b64 s[4:5], vcc
	s_cbranch_execz .LBB0_1221
	s_add_i32 s44, s20, 0x900
	s_lshl_b64 s[6:7], s[44:45], 2
	s_add_u32 s6, s92, s6
	s_addc_u32 s7, s93, s7
	s_bcnt1_i32_b64 s2, s[2:3]
	v_mov_b32_e32 v0, s2
.LBB0_1221:
	s_or_b64 exec, exec, s[4:5]
	s_waitcnt vmcnt(0)

; __device__ __forceinline__ unsigned xb_ld(unsigned* p)              { return __hip_atomic_load(p, __ATOMIC_RELAXED, __HIP_MEMORY_SCOPE_AGENT); }
; __device__ __forceinline__ unsigned xb_add(unsigned* p, unsigned v) { return __hip_atomic_fetch_add(p, v, __ATOMIC_RELAXED, __HIP_MEMORY_SCOPE_AGENT); }
; #define XB_SPIN(cond, bar) do { unsigned _sp = 0; while (cond) { __builtin_amdgcn_s_sleep(1); \
;     if ((++_sp & 255u) == 0u) { if (xb_ld(&(bar)[XB_TMO])) break; if (_sp > XB_SPIN_CAP) { atomicAdd(&(bar)[XB_TMO], 1u); break; } } } } while (0)
; __device__ __forceinline__ void xcd_barrier(const XcdBarrier& b) {
;     ...
;             else XB_SPIN(xb_ld(&bar[XB_TOPGEN]) == tg, bar);
;             __builtin_amdgcn_fence(__ATOMIC_ACQUIRE, "agent");
;             xb_add(&bar[XB_XGEN(b.x)], 1u);
;             asm volatile("s_waitcnt vmcnt(0)" ::: "memory");
.LBB0_1323:
	s_or_b64 exec, exec, s[4:5]
	s_mov_b64 s[4:5], exec
	v_mbcnt_lo_u32_b32 v0, s4, 0
	v_mbcnt_hi_u32_b32 v0, s5, v0
	v_cmp_eq_u32_e32 vcc, 0, v0
	s_waitcnt vmcnt(0)
	buffer_inv sc1
	s_and_saveexec_b64 s[6:7], vcc
	s_cbranch_execz .LBB0_1325
	s_add_i32 s44, s23, 0x900
	s_lshl_b64 s[8:9], s[44:45], 2
	s_add_u32 s8, s92, s8
	s_addc_u32 s9, s93, s9
	s_bcnt1_i32_b64 s4, s[4:5]
	v_mov_b32_e32 v0, s4
.LBB0_1325:
	s_or_b64 exec, exec, s[6:7]
	s_waitcnt vmcnt(0)

; __device__ __forceinline__ unsigned xb_ld(unsigned* p)              { return __hip_atomic_load(p, __ATOMIC_RELAXED, __HIP_MEMORY_SCOPE_AGENT); }
; __device__ __forceinline__ unsigned xb_add(unsigned* p, unsigned v) { return __hip_atomic_fetch_add(p, v, __ATOMIC_RELAXED, __HIP_MEMORY_SCOPE_AGENT); }
; #define XB_SPIN(cond, bar) do { unsigned _sp = 0; while (cond) { __builtin_amdgcn_s_sleep(1); \
;     if ((++_sp & 255u) == 0u) { if (xb_ld(&(bar)[XB_TMO])) break; if (_sp > XB_SPIN_CAP) { atomicAdd(&(bar)[XB_TMO], 1u); break; } } } } while (0)
; __device__ __forceinline__ void xcd_barrier(const XcdBarrier& b) {
;     ...
;             else XB_SPIN(xb_ld(&bar[XB_TOPGEN]) == tg, bar);
;             __builtin_amdgcn_fence(__ATOMIC_ACQUIRE, "agent");
;             xb_add(&bar[XB_XGEN(b.x)], 1u);
;             asm volatile("s_waitcnt vmcnt(0)" ::: "memory");
.LBB0_1408:
	s_or_b64 exec, exec, s[2:3]
	s_mov_b64 s[2:3], exec
	v_mbcnt_lo_u32_b32 v0, s2, 0
	v_mbcnt_hi_u32_b32 v0, s3, v0
	v_cmp_eq_u32_e32 vcc, 0, v0
	s_waitcnt vmcnt(0)
	buffer_inv sc1
	s_and_saveexec_b64 s[4:5], vcc
	s_cbranch_execz .LBB0_1410
	s_add_i32 s44, s20, 0x900
	s_lshl_b64 s[6:7], s[44:45], 2
	s_add_u32 s6, s92, s6
	s_addc_u32 s7, s93, s7
	s_bcnt1_i32_b64 s2, s[2:3]
	v_mov_b32_e32 v0, s2
.LBB0_1410:
	s_or_b64 exec, exec, s[4:5]
	s_waitcnt vmcnt(0)

; __device__ __forceinline__ unsigned xb_ld(unsigned* p)              { return __hip_atomic_load(p, __ATOMIC_RELAXED, __HIP_MEMORY_SCOPE_AGENT); }
; __device__ __forceinline__ unsigned xb_add(unsigned* p, unsigned v) { return __hip_atomic_fetch_add(p, v, __ATOMIC_RELAXED, __HIP_MEMORY_SCOPE_AGENT); }
; #define XB_SPIN(cond, bar) do { unsigned _sp = 0; while (cond) { __builtin_amdgcn_s_sleep(1); \
;     if ((++_sp & 255u) == 0u) { if (xb_ld(&(bar)[XB_TMO])) break; if (_sp > XB_SPIN_CAP) { atomicAdd(&(bar)[XB_TMO], 1u); break; } } } } while (0)
; __device__ __forceinline__ void xcd_barrier(const XcdBarrier& b) {
;     ...
;             else XB_SPIN(xb_ld(&bar[XB_TOPGEN]) == tg, bar);
;             __builtin_amdgcn_fence(__ATOMIC_ACQUIRE, "agent");
;             xb_add(&bar[XB_XGEN(b.x)], 1u);
;             asm volatile("s_waitcnt vmcnt(0)" ::: "memory");
.LBB0_1778:
	s_or_b64 exec, exec, s[4:5]
	s_mov_b64 s[4:5], exec
	v_mbcnt_lo_u32_b32 v0, s4, 0
	v_mbcnt_hi_u32_b32 v0, s5, v0
	v_cmp_eq_u32_e32 vcc, 0, v0
	s_waitcnt vmcnt(0)
	buffer_inv sc1
	s_and_saveexec_b64 s[6:7], vcc
	s_cbranch_execz .LBB0_1780
	s_add_i32 s44, s23, 0x900
	s_lshl_b64 s[8:9], s[44:45], 2
	s_add_u32 s8, s92, s8
	s_addc_u32 s9, s93, s9
	s_bcnt1_i32_b64 s4, s[4:5]
	v_mov_b32_e32 v0, s4
.LBB0_1780:
	s_or_b64 exec, exec, s[6:7]
	s_waitcnt vmcnt(0)

; __device__ __forceinline__ unsigned xb_ld(unsigned* p)              { return __hip_atomic_load(p, __ATOMIC_RELAXED, __HIP_MEMORY_SCOPE_AGENT); }
; __device__ __forceinline__ unsigned xb_add(unsigned* p, unsigned v) { return __hip_atomic_fetch_add(p, v, __ATOMIC_RELAXED, __HIP_MEMORY_SCOPE_AGENT); }
; #define XB_SPIN(cond, bar) do { unsigned _sp = 0; while (cond) { __builtin_amdgcn_s_sleep(1); \
;     if ((++_sp & 255u) == 0u) { if (xb_ld(&(bar)[XB_TMO])) break; if (_sp > XB_SPIN_CAP) { atomicAdd(&(bar)[XB_TMO], 1u); break; } } } } while (0)
; __device__ __forceinline__ void xcd_barrier(const XcdBarrier& b) {
;     ...
;             else XB_SPIN(xb_ld(&bar[XB_TOPGEN]) == tg, bar);
;             __builtin_amdgcn_fence(__ATOMIC_ACQUIRE, "agent");
;             xb_add(&bar[XB_XGEN(b.x)], 1u);
;             asm volatile("s_waitcnt vmcnt(0)" ::: "memory");
.LBB0_2299:
	s_or_b64 exec, exec, s[4:5]
	s_mov_b64 s[4:5], exec
	v_mbcnt_lo_u32_b32 v0, s4, 0
	v_mbcnt_hi_u32_b32 v0, s5, v0
	v_cmp_eq_u32_e32 vcc, 0, v0
	s_waitcnt vmcnt(0)
	buffer_inv sc1
	s_and_saveexec_b64 s[6:7], vcc
	s_cbranch_execz .LBB0_2301
	s_add_i32 s44, s23, 0x900
	s_lshl_b64 s[8:9], s[44:45], 2
	s_add_u32 s8, s92, s8
	s_addc_u32 s9, s93, s9
	s_bcnt1_i32_b64 s4, s[4:5]
	v_mov_b32_e32 v0, s4
.LBB0_2301:
	s_or_b64 exec, exec, s[6:7]
	s_waitcnt vmcnt(0)

; __device__ __forceinline__ unsigned xb_ld(unsigned* p)              { return __hip_atomic_load(p, __ATOMIC_RELAXED, __HIP_MEMORY_SCOPE_AGENT); }
; __device__ __forceinline__ unsigned xb_add(unsigned* p, unsigned v) { return __hip_atomic_fetch_add(p, v, __ATOMIC_RELAXED, __HIP_MEMORY_SCOPE_AGENT); }
; #define XB_SPIN(cond, bar) do { unsigned _sp = 0; while (cond) { __builtin_amdgcn_s_sleep(1); \
;     if ((++_sp & 255u) == 0u) { if (xb_ld(&(bar)[XB_TMO])) break; if (_sp > XB_SPIN_CAP) { atomicAdd(&(bar)[XB_TMO], 1u); break; } } } } while (0)
; __device__ __forceinline__ void xcd_barrier(const XcdBarrier& b) {
;     ...
;             else XB_SPIN(xb_ld(&bar[XB_TOPGEN]) == tg, bar);
;             __builtin_amdgcn_fence(__ATOMIC_ACQUIRE, "agent");
;             xb_add(&bar[XB_XGEN(b.x)], 1u);
;             asm volatile("s_waitcnt vmcnt(0)" ::: "memory");
.LBB0_2390:
	s_or_b64 exec, exec, s[4:5]
	s_mov_b64 s[4:5], exec
	v_mbcnt_lo_u32_b32 v0, s4, 0
	v_mbcnt_hi_u32_b32 v0, s5, v0
	v_cmp_eq_u32_e32 vcc, 0, v0
	s_waitcnt vmcnt(0)
	buffer_inv sc1
	s_and_saveexec_b64 s[6:7], vcc
	s_cbranch_execz .LBB0_2392
	s_add_i32 s44, s23, 0x900
	s_lshl_b64 s[8:9], s[44:45], 2
	s_add_u32 s8, s92, s8
	s_addc_u32 s9, s93, s9
	s_bcnt1_i32_b64 s4, s[4:5]
	v_mov_b32_e32 v0, s4
.LBB0_2392:
	s_or_b64 exec, exec, s[6:7]
	s_waitcnt vmcnt(0)

; __device__ __forceinline__ unsigned xb_ld(unsigned* p)              { return __hip_atomic_load(p, __ATOMIC_RELAXED, __HIP_MEMORY_SCOPE_AGENT); }
; __device__ __forceinline__ unsigned xb_add(unsigned* p, unsigned v) { return __hip_atomic_fetch_add(p, v, __ATOMIC_RELAXED, __HIP_MEMORY_SCOPE_AGENT); }
; #define XB_SPIN(cond, bar) do { unsigned _sp = 0; while (cond) { __builtin_amdgcn_s_sleep(1); \
;     if ((++_sp & 255u) == 0u) { if (xb_ld(&(bar)[XB_TMO])) break; if (_sp > XB_SPIN_CAP) { atomicAdd(&(bar)[XB_TMO], 1u); break; } } } } while (0)
; __device__ __forceinline__ void xcd_barrier(const XcdBarrier& b) {
;     ...
;             else XB_SPIN(xb_ld(&bar[XB_TOPGEN]) == tg, bar);
;             __builtin_amdgcn_fence(__ATOMIC_ACQUIRE, "agent");
;             xb_add(&bar[XB_XGEN(b.x)], 1u);
;             asm volatile("s_waitcnt vmcnt(0)" ::: "memory");
.LBB0_2467:
	s_or_b64 exec, exec, s[4:5]
	s_mov_b64 s[4:5], exec
	v_mbcnt_lo_u32_b32 v0, s4, 0
	v_mbcnt_hi_u32_b32 v0, s5, v0
	v_cmp_eq_u32_e32 vcc, 0, v0
	s_waitcnt vmcnt(0)
	buffer_inv sc1
	s_and_saveexec_b64 s[6:7], vcc
	s_cbranch_execz .LBB0_2469
	s_add_i32 s44, s23, 0x900
	s_lshl_b64 s[8:9], s[44:45], 2
	s_add_u32 s8, s92, s8
	s_addc_u32 s9, s93, s9
	s_bcnt1_i32_b64 s4, s[4:5]
	v_mov_b32_e32 v0, s4
.LBB0_2469:
	s_or_b64 exec, exec, s[6:7]
	s_waitcnt vmcnt(0)

; __device__ __forceinline__ unsigned xb_ld(unsigned* p)              { return __hip_atomic_load(p, __ATOMIC_RELAXED, __HIP_MEMORY_SCOPE_AGENT); }
; __device__ __forceinline__ unsigned xb_add(unsigned* p, unsigned v) { return __hip_atomic_fetch_add(p, v, __ATOMIC_RELAXED, __HIP_MEMORY_SCOPE_AGENT); }
; #define XB_SPIN(cond, bar) do { unsigned _sp = 0; while (cond) { __builtin_amdgcn_s_sleep(1); \
;     if ((++_sp & 255u) == 0u) { if (xb_ld(&(bar)[XB_TMO])) break; if (_sp > XB_SPIN_CAP) { atomicAdd(&(bar)[XB_TMO], 1u); break; } } } } while (0)
; __device__ __forceinline__ void xcd_barrier(const XcdBarrier& b) {
;     ...
;             else XB_SPIN(xb_ld(&bar[XB_TOPGEN]) == tg, bar);
;             __builtin_amdgcn_fence(__ATOMIC_ACQUIRE, "agent");
;             xb_add(&bar[XB_XGEN(b.x)], 1u);
;             asm volatile("s_waitcnt vmcnt(0)" ::: "memory");
.LBB0_2544:
	s_or_b64 exec, exec, s[4:5]
	s_mov_b64 s[4:5], exec
	v_mbcnt_lo_u32_b32 v0, s4, 0
	v_mbcnt_hi_u32_b32 v0, s5, v0
	v_cmp_eq_u32_e32 vcc, 0, v0
	s_waitcnt vmcnt(0)
	buffer_inv sc1
	s_and_saveexec_b64 s[6:7], vcc
	s_cbranch_execz .LBB0_2546
	s_add_i32 s44, s23, 0x900
	s_lshl_b64 s[8:9], s[44:45], 2
	s_add_u32 s8, s92, s8
	s_addc_u32 s9, s93, s9
	s_bcnt1_i32_b64 s4, s[4:5]
	v_mov_b32_e32 v0, s4
.LBB0_2546:
	s_or_b64 exec, exec, s[6:7]
	s_waitcnt vmcnt(0)

; __device__ __forceinline__ unsigned xb_ld(unsigned* p)              { return __hip_atomic_load(p, __ATOMIC_RELAXED, __HIP_MEMORY_SCOPE_AGENT); }
; __device__ __forceinline__ unsigned xb_add(unsigned* p, unsigned v) { return __hip_atomic_fetch_add(p, v, __ATOMIC_RELAXED, __HIP_MEMORY_SCOPE_AGENT); }
; #define XB_SPIN(cond, bar) do { unsigned _sp = 0; while (cond) { __builtin_amdgcn_s_sleep(1); \
;     if ((++_sp & 255u) == 0u) { if (xb_ld(&(bar)[XB_TMO])) break; if (_sp > XB_SPIN_CAP) { atomicAdd(&(bar)[XB_TMO], 1u); break; } } } } while (0)
; __device__ __forceinline__ void xcd_barrier(const XcdBarrier& b) {
;     ...
;             else XB_SPIN(xb_ld(&bar[XB_TOPGEN]) == tg, bar);
;             __builtin_amdgcn_fence(__ATOMIC_ACQUIRE, "agent");
;             xb_add(&bar[XB_XGEN(b.x)], 1u);
;             asm volatile("s_waitcnt vmcnt(0)" ::: "memory");
.LBB0_2692:
	s_or_b64 exec, exec, s[4:5]
	s_mov_b64 s[4:5], exec
	v_mbcnt_lo_u32_b32 v0, s4, 0
	v_mbcnt_hi_u32_b32 v0, s5, v0
	v_cmp_eq_u32_e32 vcc, 0, v0
	s_waitcnt vmcnt(0)
	buffer_inv sc1
	s_and_saveexec_b64 s[6:7], vcc
	s_cbranch_execz .LBB0_2694
	s_add_i32 s44, s23, 0x900
	s_lshl_b64 s[8:9], s[44:45], 2
	s_add_u32 s8, s92, s8
	s_addc_u32 s9, s93, s9
	s_bcnt1_i32_b64 s4, s[4:5]
	v_mov_b32_e32 v0, s4
.LBB0_2694:
	s_or_b64 exec, exec, s[6:7]
	s_waitcnt vmcnt(0)

; __device__ __forceinline__ unsigned xb_ld(unsigned* p)              { return __hip_atomic_load(p, __ATOMIC_RELAXED, __HIP_MEMORY_SCOPE_AGENT); }
; __device__ __forceinline__ unsigned xb_add(unsigned* p, unsigned v) { return __hip_atomic_fetch_add(p, v, __ATOMIC_RELAXED, __HIP_MEMORY_SCOPE_AGENT); }
; #define XB_SPIN(cond, bar) do { unsigned _sp = 0; while (cond) { __builtin_amdgcn_s_sleep(1); \
;     if ((++_sp & 255u) == 0u) { if (xb_ld(&(bar)[XB_TMO])) break; if (_sp > XB_SPIN_CAP) { atomicAdd(&(bar)[XB_TMO], 1u); break; } } } } while (0)
; __device__ __forceinline__ void xcd_barrier(const XcdBarrier& b) {
;     ...
;         const unsigned old = xb_add(&bar[XB_XSUB(b.x)], 1u);
;         const unsigned gen = old / nloc;
;         if (old + 1u == (gen + 1u) * nloc) {
;             __builtin_amdgcn_fence(__ATOMIC_RELEASE, "agent");
;             asm volatile("s_waitcnt vmcnt(0)" ::: "memory");
;             const unsigned og = xb_add(&bar[XB_TOP], 1u);
;             const unsigned tg = og / nx;
;             if (og + 1u == (tg + 1u) * nx) xb_add(&bar[XB_TOPGEN], 1u);
;             else XB_SPIN(xb_ld(&bar[XB_TOPGEN]) == tg, bar);
;             __builtin_amdgcn_fence(__ATOMIC_ACQUIRE, "agent");
;             xb_add(&bar[XB_XGEN(b.x)], 1u);
;             asm volatile("s_waitcnt vmcnt(0)" ::: "memory");
;         } else {
;             XB_SPIN(xb_ld(&bar[XB_XGEN(b.x)]) == gen, bar);
.LBB0_2744:
	s_or_b64 exec, exec, s[6:7]
	v_cvt_f32_u32_e32 v4, v2
	s_waitcnt vmcnt(0)
	v_readfirstlane_b32 s4, v3
	v_sub_u32_e32 v3, 0, v2
	v_rcp_iflag_f32_e32 v4, v4
	v_add_u32_e32 v5, s4, v1
	v_mul_f32_e32 v4, 0x4f7ffffe, v4
	v_cvt_u32_f32_e32 v4, v4
	v_mul_lo_u32 v1, v3, v4
	v_mul_hi_u32 v1, v4, v1
	v_add_u32_e32 v1, v4, v1
	v_mul_hi_u32 v1, v5, v1
	v_mul_lo_u32 v3, v1, v2
	v_sub_u32_e32 v3, v5, v3
	v_add_u32_e32 v4, 1, v1
	v_cmp_ge_u32_e32 vcc, v3, v2
	s_nop 1
	v_cndmask_b32_e32 v1, v1, v4, vcc
	v_sub_u32_e32 v4, v3, v2
	v_cndmask_b32_e32 v3, v3, v4, vcc
	v_add_u32_e32 v4, 1, v1
	v_cmp_ge_u32_e32 vcc, v3, v2
	v_add_u32_e32 v3, 1, v5
	s_nop 0
	v_cndmask_b32_e32 v1, v1, v4, vcc
	v_mul_lo_u32 v4, v2, v1
	v_add_u32_e32 v2, v4, v2
	v_cmp_ne_u32_e32 vcc, v3, v2
	s_and_saveexec_b64 s[4:5], vcc
	s_xor_b64 s[4:5], exec, s[4:5]
	s_cbranch_execz .LBB0_2758
	s_add_i32 s44, s22, 0x900
	s_lshl_b64 s[6:7], s[44:45], 2
	s_add_u32 s8, s92, s6
	s_addc_u32 s9, s93, s7
	s_waitcnt lgkmcnt(0)
	global_load_dword v0, v65, s[8:9] sc1
	s_waitcnt vmcnt(0)
	v_cmp_eq_u32_e32 vcc, v0, v1
	s_and_saveexec_b64 s[6:7], vcc
	s_cbranch_execz .LBB0_2757
	s_mov_b32 s20, 1
	s_mov_b64 s[10:11], 0
	s_branch .LBB0_2748

; __device__ __forceinline__ unsigned xb_ld(unsigned* p)              { return __hip_atomic_load(p, __ATOMIC_RELAXED, __HIP_MEMORY_SCOPE_AGENT); }
; __device__ __forceinline__ unsigned xb_add(unsigned* p, unsigned v) { return __hip_atomic_fetch_add(p, v, __ATOMIC_RELAXED, __HIP_MEMORY_SCOPE_AGENT); }
; #define XB_SPIN(cond, bar) do { unsigned _sp = 0; while (cond) { __builtin_amdgcn_s_sleep(1); \
;     if ((++_sp & 255u) == 0u) { if (xb_ld(&(bar)[XB_TMO])) break; if (_sp > XB_SPIN_CAP) { atomicAdd(&(bar)[XB_TMO], 1u); break; } } } } while (0)
; __device__ __forceinline__ void xcd_barrier(const XcdBarrier& b) {
;     ...
;             if (og + 1u == (tg + 1u) * nx) xb_add(&bar[XB_TOPGEN], 1u);
;             else XB_SPIN(xb_ld(&bar[XB_TOPGEN]) == tg, bar);
;             __builtin_amdgcn_fence(__ATOMIC_ACQUIRE, "agent");
;             xb_add(&bar[XB_XGEN(b.x)], 1u);
.Lxrel_skip_11:
	s_and_saveexec_b64 s[6:7], vcc
	s_cbranch_execz .LBB0_2773
	s_add_i32 s44, s22, 0x900
	s_lshl_b64 s[4:5], s[44:45], 2
	s_add_u32 s4, s92, s4
	s_addc_u32 s5, s93, s5
	global_load_dword v0, v65, s[4:5] sc1
	s_mov_b64 s[12:13], 0
	s_waitcnt vmcnt(0)
	v_cmp_eq_u32_e32 vcc, v0, v2
	s_and_saveexec_b64 s[10:11], vcc
	s_cbranch_execz .LBB0_2772
	s_add_u32 s8, s92, 0x200
	s_addc_u32 s9, s93, 0
	s_mov_b32 s23, 1
	s_branch .LBB0_2765

; __device__ __forceinline__ unsigned xb_ld(unsigned* p)              { return __hip_atomic_load(p, __ATOMIC_RELAXED, __HIP_MEMORY_SCOPE_AGENT); }
; __device__ __forceinline__ unsigned xb_add(unsigned* p, unsigned v) { return __hip_atomic_fetch_add(p, v, __ATOMIC_RELAXED, __HIP_MEMORY_SCOPE_AGENT); }
; #define XB_SPIN(cond, bar) do { unsigned _sp = 0; while (cond) { __builtin_amdgcn_s_sleep(1); \
;     if ((++_sp & 255u) == 0u) { if (xb_ld(&(bar)[XB_TMO])) break; if (_sp > XB_SPIN_CAP) { atomicAdd(&(bar)[XB_TMO], 1u); break; } } } } while (0)
; __device__ __forceinline__ void xcd_barrier(const XcdBarrier& b) {
;     ...
;             else XB_SPIN(xb_ld(&bar[XB_TOPGEN]) == tg, bar);
;             __builtin_amdgcn_fence(__ATOMIC_ACQUIRE, "agent");
;             xb_add(&bar[XB_XGEN(b.x)], 1u);
;             asm volatile("s_waitcnt vmcnt(0)" ::: "memory");
.LBB0_2775:
	s_or_b64 exec, exec, s[4:5]
	s_mov_b64 s[4:5], exec
	v_mbcnt_lo_u32_b32 v0, s4, 0
	v_mbcnt_hi_u32_b32 v0, s5, v0
	v_cmp_eq_u32_e32 vcc, 0, v0
	s_waitcnt vmcnt(0)
	buffer_inv sc1
	s_and_saveexec_b64 s[6:7], vcc
	s_cbranch_execz .LBB0_2777
	s_add_i32 s44, s22, 0x900
	s_lshl_b64 s[8:9], s[44:45], 2
	s_add_u32 s8, s92, s8
	s_addc_u32 s9, s93, s9
	s_bcnt1_i32_b64 s4, s[4:5]
	v_mov_b32_e32 v0, s4
.LBB0_2777:
	s_or_b64 exec, exec, s[6:7]
	s_waitcnt vmcnt(0)

; __device__ __forceinline__ unsigned xb_ld(unsigned* p)              { return __hip_atomic_load(p, __ATOMIC_RELAXED, __HIP_MEMORY_SCOPE_AGENT); }
; __device__ __forceinline__ unsigned xb_add(unsigned* p, unsigned v) { return __hip_atomic_fetch_add(p, v, __ATOMIC_RELAXED, __HIP_MEMORY_SCOPE_AGENT); }
; #define XB_SPIN(cond, bar) do { unsigned _sp = 0; while (cond) { __builtin_amdgcn_s_sleep(1); \
;     if ((++_sp & 255u) == 0u) { if (xb_ld(&(bar)[XB_TMO])) break; if (_sp > XB_SPIN_CAP) { atomicAdd(&(bar)[XB_TMO], 1u); break; } } } } while (0)
; __device__ __forceinline__ void xcd_barrier(const XcdBarrier& b) {
;     ...
;             else XB_SPIN(xb_ld(&bar[XB_TOPGEN]) == tg, bar);
;             __builtin_amdgcn_fence(__ATOMIC_ACQUIRE, "agent");
;             xb_add(&bar[XB_XGEN(b.x)], 1u);
;             asm volatile("s_waitcnt vmcnt(0)" ::: "memory");
.LBB0_2990:
	s_or_b64 exec, exec, s[4:5]
	s_mov_b64 s[4:5], exec
	v_mbcnt_lo_u32_b32 v0, s4, 0
	v_mbcnt_hi_u32_b32 v0, s5, v0
	v_cmp_eq_u32_e32 vcc, 0, v0
	s_waitcnt vmcnt(0)
	buffer_inv sc1
	s_and_saveexec_b64 s[6:7], vcc
	s_cbranch_execz .LBB0_2992
	s_add_i32 s44, s23, 0x900
	s_lshl_b64 s[8:9], s[44:45], 2
	s_add_u32 s8, s92, s8
	s_addc_u32 s9, s93, s9
	s_bcnt1_i32_b64 s4, s[4:5]
	v_mov_b32_e32 v0, s4
.LBB0_2992:
	s_or_b64 exec, exec, s[6:7]
	s_waitcnt vmcnt(0)

; __device__ __forceinline__ unsigned xb_ld(unsigned* p)              { return __hip_atomic_load(p, __ATOMIC_RELAXED, __HIP_MEMORY_SCOPE_AGENT); }
; __device__ __forceinline__ unsigned xb_add(unsigned* p, unsigned v) { return __hip_atomic_fetch_add(p, v, __ATOMIC_RELAXED, __HIP_MEMORY_SCOPE_AGENT); }
; #define XB_SPIN(cond, bar) do { unsigned _sp = 0; while (cond) { __builtin_amdgcn_s_sleep(1); \
;     if ((++_sp & 255u) == 0u) { if (xb_ld(&(bar)[XB_TMO])) break; if (_sp > XB_SPIN_CAP) { atomicAdd(&(bar)[XB_TMO], 1u); break; } } } } while (0)
; __device__ __forceinline__ void xcd_barrier(const XcdBarrier& b) {
;     ...
;             else XB_SPIN(xb_ld(&bar[XB_TOPGEN]) == tg, bar);
;             __builtin_amdgcn_fence(__ATOMIC_ACQUIRE, "agent");
;             xb_add(&bar[XB_XGEN(b.x)], 1u);
;             asm volatile("s_waitcnt vmcnt(0)" ::: "memory");
.LBB0_3071:
	s_or_b64 exec, exec, s[4:5]
	s_mov_b64 s[4:5], exec
	v_mbcnt_lo_u32_b32 v0, s4, 0
	v_mbcnt_hi_u32_b32 v0, s5, v0
	v_cmp_eq_u32_e32 vcc, 0, v0
	s_waitcnt vmcnt(0)
	buffer_inv sc1
	s_and_saveexec_b64 s[6:7], vcc
	s_cbranch_execz .LBB0_3073
	s_add_i32 s44, s23, 0x900
	s_lshl_b64 s[8:9], s[44:45], 2
	s_add_u32 s8, s92, s8
	s_addc_u32 s9, s93, s9
	s_bcnt1_i32_b64 s4, s[4:5]
	v_mov_b32_e32 v0, s4
.LBB0_3073:
	s_or_b64 exec, exec, s[6:7]
	s_waitcnt vmcnt(0)

; __device__ __forceinline__ unsigned xb_ld(unsigned* p)              { return __hip_atomic_load(p, __ATOMIC_RELAXED, __HIP_MEMORY_SCOPE_AGENT); }
; __device__ __forceinline__ unsigned xb_add(unsigned* p, unsigned v) { return __hip_atomic_fetch_add(p, v, __ATOMIC_RELAXED, __HIP_MEMORY_SCOPE_AGENT); }
; #define XB_SPIN(cond, bar) do { unsigned _sp = 0; while (cond) { __builtin_amdgcn_s_sleep(1); \
;     if ((++_sp & 255u) == 0u) { if (xb_ld(&(bar)[XB_TMO])) break; if (_sp > XB_SPIN_CAP) { atomicAdd(&(bar)[XB_TMO], 1u); break; } } } } while (0)
; __device__ __forceinline__ void xcd_barrier(const XcdBarrier& b) {
;     ...
;             else XB_SPIN(xb_ld(&bar[XB_TOPGEN]) == tg, bar);
;             __builtin_amdgcn_fence(__ATOMIC_ACQUIRE, "agent");
;             xb_add(&bar[XB_XGEN(b.x)], 1u);
;             asm volatile("s_waitcnt vmcnt(0)" ::: "memory");
.LBB0_3784:
	s_add_i32 s44, s20, 0x900
	s_lshl_b64 s[6:7], s[44:45], 2
	s_add_u32 s6, s92, s6
	s_addc_u32 s7, s93, s7
	s_bcnt1_i32_b64 s2, s[2:3]
	v_mov_b32_e32 v0, s2
	s_getpc_b64 s[98:99]
